# baseline (speedup 1.0000x reference)
_Z6gat_k1PKfS0_S0_S0_PDF16_S1_S1_Pf:
	s_load_dwordx8 s[4:11], s[0:1], 0x0
	s_load_dwordx8 s[12:19], s[0:1], 0x20
	v_lshrrev_b32_e32 v54, 6, v0
	v_bfe_u32 v123, v0, 4, 2
	v_and_b32_e32 v120, 15, v0
	v_lshlrev_b32_e32 v120, 4, v120
	v_lshl_or_b32 v120, v54, 8, v120
	v_mov_b32_e32 v121, 0
	v_and_b32_e32 v57, 0xc0, v0
	s_lshl_b32 s3, s2, 5
	v_and_b32_e32 v1, 63, v0
	v_bfe_u32 v55, v0, 5, 1
	v_lshlrev_b32_e32 v2, 8, v57
	v_mov_b32_e32 v19, 0
	v_or_b32_e32 v4, s3, v123
	v_and_b32_e32 v56, 31, v0
	v_lshl_or_b32 v18, v55, 11, v2
	v_lshlrev_b32_e32 v20, 4, v1
	v_mov_b32_e32 v21, v19
	v_ashrrev_i32_e32 v5, 31, v4
	s_waitcnt lgkmcnt(0)
	v_lshl_add_u64 v[2:3], s[6:7], 0, v[18:19]
	v_lshlrev_b32_e32 v18, 2, v56
	s_lshl_b32 s20, s3, 10
	s_add_u32 s20, s4, s20
	s_addc_u32 s21, s5, 0
	v_lshl_or_b32 v121, v123, 10, v120
	global_load_dwordx4 v[22:25], v121, s[20:21] nt
	s_add_u32 s20, s20, 0x1000
	s_addc_u32 s21, s21, 0
	global_load_dwordx4 v[26:29], v121, s[20:21] nt
	s_add_u32 s20, s20, 0x1000
	s_addc_u32 s21, s21, 0
	global_load_dwordx4 v[30:33], v121, s[20:21] nt
	s_add_u32 s20, s20, 0x1000
	s_addc_u32 s21, s21, 0
	global_load_dwordx4 v[34:37], v121, s[20:21] nt
	s_add_u32 s20, s20, 0x1000
	s_addc_u32 s21, s21, 0
	global_load_dwordx4 v[38:41], v121, s[20:21] nt
	s_add_u32 s20, s20, 0x1000
	s_addc_u32 s21, s21, 0
	global_load_dwordx4 v[42:45], v121, s[20:21] nt
	s_add_u32 s20, s20, 0x1000
	s_addc_u32 s21, s21, 0
	global_load_dwordx4 v[46:49], v121, s[20:21] nt
	s_add_u32 s20, s20, 0x1000
	s_addc_u32 s21, s21, 0
	global_load_dwordx4 v[50:53], v121, s[20:21] nt
	s_movk_i32 s4, 0x410
	v_mad_u32_u24 v122, v123, s4, v120
	v_lshl_add_u64 v[2:3], v[2:3], 0, v[18:19]
	v_lshl_add_u64 v[2:3], v[2:3], 0, v[18:19]
	s_movk_i32 s22, 0x1000
	s_mov_b32 s23, 0
	v_lshl_add_u64 v[4:5], v[2:3], 0, s[22:23]
	s_movk_i32 s22, 0x3000
	v_lshl_add_u64 v[6:7], v[2:3], 0, s[22:23]
	global_load_dwordx2 v[58:59], v[4:5], off offset:-4096
	global_load_dwordx2 v[60:61], v[4:5], off offset:-3840
	global_load_dwordx2 v[62:63], v[4:5], off offset:-3584
	global_load_dwordx2 v[64:65], v[4:5], off offset:-3328
	global_load_dwordx2 v[66:67], v[4:5], off offset:-3072
	global_load_dwordx2 v[68:69], v[4:5], off offset:-2816
	global_load_dwordx2 v[70:71], v[4:5], off offset:-2560
	global_load_dwordx2 v[72:73], v[4:5], off offset:-2304
	global_load_dwordx2 v[74:75], v[4:5], off
	global_load_dwordx2 v[76:77], v[4:5], off offset:256
	global_load_dwordx2 v[78:79], v[4:5], off offset:512
	global_load_dwordx2 v[80:81], v[4:5], off offset:768
	global_load_dwordx2 v[82:83], v[4:5], off offset:1024
	global_load_dwordx2 v[84:85], v[4:5], off offset:1280
	global_load_dwordx2 v[86:87], v[4:5], off offset:1536
	global_load_dwordx2 v[88:89], v[4:5], off offset:1792
	global_load_dwordx2 v[90:91], v[6:7], off offset:-4096
	global_load_dwordx2 v[92:93], v[6:7], off offset:-3840
	global_load_dwordx2 v[94:95], v[6:7], off offset:-3584
	global_load_dwordx2 v[96:97], v[6:7], off offset:-3328
	global_load_dwordx2 v[98:99], v[6:7], off offset:-3072
	global_load_dwordx2 v[100:101], v[6:7], off offset:-2816
	global_load_dwordx2 v[102:103], v[6:7], off offset:-2560
	global_load_dwordx2 v[104:105], v[6:7], off offset:-2304
	global_load_dwordx2 v[106:107], v[6:7], off
	global_load_dwordx2 v[108:109], v[6:7], off offset:256
	global_load_dwordx2 v[110:111], v[6:7], off offset:512
	global_load_dwordx2 v[112:113], v[6:7], off offset:768
	global_load_dwordx2 v[114:115], v[6:7], off offset:1024
	global_load_dwordx2 v[116:117], v[6:7], off offset:1280
	global_load_dwordx2 v[118:119], v[6:7], off offset:1536
	global_load_dwordx2 v[120:121], v[6:7], off offset:1792
	v_and_b32_e32 v1, 7, v0
	v_lshlrev_b32_e32 v123, 5, v1
	global_load_dwordx4 v[6:9], v123, s[8:9]
	global_load_dwordx4 v[2:5], v123, s[10:11]
	global_load_dwordx4 v[14:17], v123, s[8:9] offset:16
	global_load_dwordx4 v[10:13], v123, s[10:11] offset:16
	s_movk_i32 s8, 0x110
	s_waitcnt vmcnt(36)
	ds_write_b128 v122, v[22:25] offset:34816
	ds_write_b128 v122, v[26:29] offset:38976
	ds_write_b128 v122, v[30:33] offset:43136
	ds_write_b128 v122, v[34:37] offset:47296
	ds_write_b128 v122, v[38:41] offset:51456
	ds_write_b128 v122, v[42:45] offset:55616
	s_waitcnt vmcnt(36)
	ds_write_b128 v122, v[46:49] offset:59776
	s_waitcnt vmcnt(36)
	ds_write_b128 v122, v[50:53] offset:63936
	v_mul_u32_u24_e32 v22, 0x410, v56
	v_lshlrev_b32_e32 v23, 2, v57
	v_and_b32_e32 v24, 32, v0
	v_add3_u32 v38, v22, v23, v24
	s_waitcnt lgkmcnt(0)
	ds_read_b128 v[22:25], v38 offset:34832
	ds_read_b128 v[26:29], v38 offset:34816
	ds_read_b128 v[30:33], v38 offset:34880
	ds_read_b128 v[34:37], v38 offset:34896
	s_waitcnt lgkmcnt(3)
	v_cvt_pk_f16_f32 v25, v24, v25
	v_cvt_pk_f16_f32 v24, v22, v23
	s_waitcnt lgkmcnt(2)
	v_cvt_pk_f16_f32 v23, v28, v29
	v_cvt_pk_f16_f32 v22, v26, v27
	s_waitcnt vmcnt(28)
	v_cvt_pk_f16_f32 v29, v70, v72
	v_cvt_pk_f16_f32 v28, v66, v68
	v_cvt_pk_f16_f32 v27, v62, v64
	v_cvt_pk_f16_f32 v26, v58, v60
	v_lshlrev_b32_e32 v19, 2, v55
	s_nop 0
	v_mfma_f32_32x32x16_f16 a[0:15], v[22:25], v[26:29], 0
	s_waitcnt vmcnt(28)
	v_cvt_pk_f16_f32 v29, v71, v73
	v_cvt_pk_f16_f32 v28, v67, v69
	v_cvt_pk_f16_f32 v27, v63, v65
	v_cvt_pk_f16_f32 v26, v59, v61
	s_nop 1
	v_mfma_f32_32x32x16_f16 a[16:31], v[22:25], v[26:29], 0
	s_waitcnt lgkmcnt(0)
	v_cvt_pk_f16_f32 v25, v36, v37
	v_cvt_pk_f16_f32 v24, v34, v35
	v_cvt_pk_f16_f32 v23, v32, v33
	v_cvt_pk_f16_f32 v22, v30, v31
	ds_read_b128 v[30:33], v38 offset:34944
	ds_read_b128 v[34:37], v38 offset:34960
	s_waitcnt vmcnt(20)
	v_cvt_pk_f16_f32 v29, v86, v88
	v_cvt_pk_f16_f32 v28, v82, v84
	v_cvt_pk_f16_f32 v27, v78, v80
	s_waitcnt vmcnt(20)
	v_cvt_pk_f16_f32 v26, v74, v76
	s_nop 1
	v_mfma_f32_32x32x16_f16 a[0:15], v[22:25], v[26:29], a[0:15]
	v_cvt_pk_f16_f32 v29, v87, v89
	v_cvt_pk_f16_f32 v28, v83, v85
	v_cvt_pk_f16_f32 v27, v79, v81
	v_cvt_pk_f16_f32 v26, v75, v77
	s_nop 1
	v_mfma_f32_32x32x16_f16 a[16:31], v[22:25], v[26:29], a[16:31]
	s_waitcnt lgkmcnt(0)
	v_cvt_pk_f16_f32 v25, v36, v37
	v_cvt_pk_f16_f32 v24, v34, v35
	v_cvt_pk_f16_f32 v23, v32, v33
	v_cvt_pk_f16_f32 v22, v30, v31
	ds_read_b128 v[30:33], v38 offset:35008
	ds_read_b128 v[34:37], v38 offset:35024
	s_waitcnt vmcnt(12)
	v_cvt_pk_f16_f32 v29, v102, v104
	v_cvt_pk_f16_f32 v28, v98, v100
	v_cvt_pk_f16_f32 v27, v94, v96
	v_cvt_pk_f16_f32 v26, v90, v92
	s_nop 1
	v_mfma_f32_32x32x16_f16 a[0:15], v[22:25], v[26:29], a[0:15]
	s_waitcnt vmcnt(12)
	v_cvt_pk_f16_f32 v29, v103, v105
	v_cvt_pk_f16_f32 v28, v99, v101
	v_cvt_pk_f16_f32 v27, v95, v97
	v_cvt_pk_f16_f32 v26, v91, v93
	s_nop 1
	v_mfma_f32_32x32x16_f16 a[16:31], v[22:25], v[26:29], a[16:31]
	s_waitcnt lgkmcnt(0)
	v_cvt_pk_f16_f32 v25, v36, v37
	v_cvt_pk_f16_f32 v24, v34, v35
	v_cvt_pk_f16_f32 v23, v32, v33
	v_cvt_pk_f16_f32 v22, v30, v31
	s_waitcnt vmcnt(4)
	v_cvt_pk_f16_f32 v29, v118, v120
	v_cvt_pk_f16_f32 v28, v114, v116
	v_cvt_pk_f16_f32 v27, v110, v112
	v_cvt_pk_f16_f32 v26, v106, v108
	s_nop 1
	v_mfma_f32_32x32x16_f16 a[0:15], v[22:25], v[26:29], a[0:15]
	s_waitcnt vmcnt(4)
	v_cvt_pk_f16_f32 v29, v119, v121
	v_cvt_pk_f16_f32 v28, v115, v117
	v_cvt_pk_f16_f32 v27, v111, v113
	v_cvt_pk_f16_f32 v26, v107, v109
	s_nop 1
	v_mfma_f32_32x32x16_f16 a[16:31], v[22:25], v[26:29], a[16:31]
	v_lshl_or_b32 v22, v54, 5, v19
	v_mul_u32_u24_e32 v22, 0x44, v22
	v_lshl_add_u32 v22, v22, 2, v18
	v_add_u32_e32 v22, v22, v18
	v_add_u32_e32 v23, 0x880, v22
	v_add_u32_e32 v24, 0x1100, v22
	v_add_u32_e32 v25, 0x1980, v22
	s_nop 5
	ds_write2_b32 v22, a0, a16 offset1:1
	ds_write2_b32 v22, a1, a17 offset0:68 offset1:69
	ds_write2_b32 v22, a2, a18 offset0:136 offset1:137
	ds_write2_b32 v22, a3, a19 offset0:204 offset1:205
	ds_write2_b32 v23, a4, a20 offset1:1
	ds_write2_b32 v23, a5, a21 offset0:68 offset1:69
	ds_write2_b32 v23, a6, a22 offset0:136 offset1:137
	ds_write2_b32 v23, a7, a23 offset0:204 offset1:205
	ds_write2_b32 v24, a8, a24 offset1:1
	ds_write2_b32 v24, a9, a25 offset0:68 offset1:69
	ds_write2_b32 v24, a10, a26 offset0:136 offset1:137
	ds_write2_b32 v24, a11, a27 offset0:204 offset1:205
	ds_write2_b32 v25, a12, a28 offset1:1
	ds_write2_b32 v25, a13, a29 offset0:68 offset1:69
	ds_write2_b32 v25, a14, a30 offset0:136 offset1:137
	ds_write2_b32 v25, a15, a31 offset0:204 offset1:205
	v_lshrrev_b32_e32 v22, 3, v0
	v_mad_u32_u24 v23, v22, s8, v123
	s_waitcnt lgkmcnt(0)
	s_barrier
	ds_read_b128 v[24:27], v23
	ds_read_b128 v[28:31], v23 offset:16
	ds_read_b128 v[32:35], v23 offset:8704
	s_waitcnt lgkmcnt(2)
	v_pk_add_f32 v[36:37], v[26:27], 0 op_sel_hi:[1,0]
	v_pk_add_f32 v[38:39], v[24:25], 0 op_sel_hi:[1,0]
	ds_read_b128 v[24:27], v23 offset:8720
	s_waitcnt lgkmcnt(2)
	v_pk_add_f32 v[40:41], v[30:31], 0 op_sel_hi:[1,0]
	v_pk_add_f32 v[42:43], v[28:29], 0 op_sel_hi:[1,0]
	ds_read_b128 v[28:31], v23 offset:17408
	s_waitcnt lgkmcnt(2)
	v_pk_add_f32 v[34:35], v[36:37], v[34:35]
	v_pk_add_f32 v[36:37], v[38:39], v[32:33]
	s_waitcnt lgkmcnt(1)
	v_pk_add_f32 v[38:39], v[40:41], v[26:27]
	v_pk_add_f32 v[40:41], v[42:43], v[24:25]
	ds_read_b128 v[24:27], v23 offset:17424
	s_waitcnt lgkmcnt(1)
	v_pk_add_f32 v[42:43], v[34:35], v[30:31]
	ds_read_b128 v[30:33], v23 offset:26112
	v_pk_add_f32 v[28:29], v[36:37], v[28:29]
	ds_read_b128 v[34:37], v23 offset:26128
	s_waitcnt lgkmcnt(2)
	v_pk_add_f32 v[40:41], v[40:41], v[24:25]
	v_pk_add_f32 v[38:39], v[38:39], v[26:27]
	s_waitcnt lgkmcnt(1)
	v_pk_add_f32 v[24:25], v[28:29], v[30:31]
	v_pk_add_f32 v[26:27], v[42:43], v[32:33]
	s_waitcnt lgkmcnt(0)
	v_pk_add_f32 v[28:29], v[40:41], v[34:35]
	v_pk_add_f32 v[30:31], v[38:39], v[36:37]
	s_waitcnt vmcnt(0)
	v_mul_f32_e32 v10, v28, v10
	v_fmac_f32_e32 v10, v24, v2
	v_mul_f32_e32 v14, v28, v14
	v_add_f32_e32 v2, 0, v10
	v_mul_f32_e32 v10, v29, v15
	v_fmac_f32_e32 v14, v24, v6
	v_fmac_f32_e32 v10, v25, v7
	v_mul_f32_e32 v7, v29, v11
	v_add_f32_e32 v6, 0, v14
	v_fmac_f32_e32 v7, v25, v3
	v_mul_f32_e32 v3, v30, v16
	v_add_f32_e32 v6, v6, v10
	v_fmac_f32_e32 v3, v26, v8
	v_add_f32_e32 v3, v6, v3
	v_mul_f32_e32 v6, v30, v12
	v_fmac_f32_e32 v6, v26, v4
	v_mul_f32_e32 v4, v31, v17
	v_fmac_f32_e32 v4, v27, v9
	v_add_f32_e32 v2, v2, v7
	v_add_f32_e32 v3, v3, v4
	v_mul_f32_e32 v4, v31, v13
	v_add_f32_e32 v2, v2, v6
	v_fmac_f32_e32 v4, v27, v5
	v_add_f32_e32 v2, v2, v4
	ds_write_b128 v23, v[24:27]
	ds_write_b128 v23, v[28:31] offset:16
	s_nop 1
	v_add_f32_dpp v3, v3, v3 quad_perm:[1,0,3,2] row_mask:0xf bank_mask:0xf
	v_add_f32_dpp v6, v2, v2 quad_perm:[1,0,3,2] row_mask:0xf bank_mask:0xf
	s_nop 1
	v_add_f32_dpp v3, v3, v3 quad_perm:[2,3,0,1] row_mask:0xf bank_mask:0xf
	v_add_f32_dpp v6, v6, v6 quad_perm:[2,3,0,1] row_mask:0xf bank_mask:0xf
	s_nop 1
	v_add_f32_dpp v2, v3, v3 row_half_mirror row_mask:0xf bank_mask:0xf
	v_add_f32_dpp v3, v6, v6 row_half_mirror row_mask:0xf bank_mask:0xf
	v_cmp_eq_u32_e32 vcc, 0, v1
	s_and_saveexec_b64 s[6:7], vcc
	s_cbranch_execz .LBB0_2
	v_mul_f32_e32 v4, 0x3f7d70a4, v3
	v_mul_f32_e32 v4, 0x3fb8aa3b, v4
	v_mul_f32_e32 v3, 0x3c23d70a, v3
	v_exp_f32_e32 v4, v4
	v_mul_f32_e32 v3, 0x3fb8aa3b, v3
	v_exp_f32_e32 v3, v3
	v_lshlrev_b32_e32 v5, 2, v22
	v_or_b32_e32 v6, 0x10a80, v5
	v_mul_f32_e32 v2, 0xbf7d70a4, v2
	ds_write_b32 v6, v4
	v_or_b32_e32 v4, 0x10a00, v5
	v_mul_f32_e32 v2, 0x3fb8aa3b, v2
	ds_write_b32 v4, v3
	v_exp_f32_e32 v4, v2
	v_add_u32_e32 v2, s3, v22
	v_ashrrev_i32_e32 v3, 31, v2
	v_lshl_add_u64 v[2:3], v[2:3], 2, s[18:19]
	global_store_dword v[2:3], v4, off
.LBB0_2:
	s_or_b64 exec, exec, s[6:7]
	v_bfe_u32 v16, v0, 6, 1
	v_lshl_or_b32 v2, v16, 4, v19
	s_movk_i32 s6, 0x80
	v_and_or_b32 v3, v0, s6, v18
	v_lshlrev_b32_e32 v6, 2, v2
	v_mad_u32_u24 v12, v2, s8, v3
	v_or_b32_e32 v2, 0x10a00, v6
	v_or_b32_e32 v6, 0x10a20, v6
	v_add_u32_e32 v14, 0x800, v12
	v_lshlrev_b32_e32 v50, 2, v0
	v_and_b32_e32 v50, 0x200, v50
	v_lshl_add_u32 v50, s2, 1, v50
	v_or_b32_e32 v50, v50, v16
	v_ashrrev_i32_e32 v51, 31, v50
	v_lshlrev_b64 v[50:51], 10, v[50:51]
	v_lshl_add_u64 v[50:51], s[12:13], 0, v[50:51]
	v_lshl_add_u64 v[50:51], v[50:51], 0, v[20:21]
	v_lshlrev_b32_e32 v40, 1, v0
	v_bfe_u32 v41, v0, 3, 1
	v_and_b32_e32 v40, 8, v40
	v_and_b32_e32 v42, 16, v0
	v_and_or_b32 v43, v0, 3, v40
	v_lshlrev_b32_e32 v40, 2, v41
	v_or3_b32 v43, v43, v40, v42
	v_lshlrev_b32_e32 v43, 2, v43
	v_or_b32_e32 v44, 0x10a80, v43
	v_or_b32_e32 v45, 0x10a00, v43
	v_lshl_or_b32 v46, v41, 3, s3
	v_or3_b32 v46, v46, v42, v1
	v_ashrrev_i32_e32 v47, 31, v46
	v_lshlrev_b64 v[46:47], 1, v[46:47]
	v_lshl_add_u64 v[48:49], s[14:15], 0, v[46:47]
	v_lshl_add_u64 v[46:47], s[16:17], 0, v[46:47]
	v_cmp_gt_u32_e32 vcc, 32, v0
	s_waitcnt lgkmcnt(0)
	s_barrier
	ds_read2_b32 v[10:11], v12 offset1:68
	ds_read_b128 v[2:5], v2
	ds_read_b128 v[6:9], v6
	ds_read2_b32 v[52:53], v12 offset0:136 offset1:204
	ds_read2_b32 v[12:13], v14 offset0:32 offset1:100
	ds_read2_b32 v[14:15], v14 offset0:168 offset1:236
	ds_read_b32 v44, v44
	ds_read_b32 v45, v45
	s_waitcnt lgkmcnt(6)
	v_pk_mul_f32 v[2:3], v[10:11], v[2:3]
	s_waitcnt lgkmcnt(4)
	v_pk_mul_f32 v[4:5], v[52:53], v[4:5]
	v_cvt_pk_f16_f32 v2, v2, v3
	v_cvt_pk_f16_f32 v3, v4, v5
	s_waitcnt lgkmcnt(3)
	v_pk_mul_f32 v[4:5], v[12:13], v[6:7]
	s_waitcnt lgkmcnt(2)
	v_pk_mul_f32 v[6:7], v[14:15], v[8:9]
	v_cvt_pk_f16_f32 v4, v4, v5
	v_cvt_pk_f16_f32 v5, v6, v7
	global_store_dwordx4 v[50:51], v[2:5], off sc1
	s_and_saveexec_b64 s[4:5], vcc
	s_cbranch_execz .LBB0_4
	s_waitcnt lgkmcnt(0)
	v_cvt_f16_f32_e32 v44, v44
	v_cvt_f16_f32_e32 v45, v45
	global_store_short v[48:49], v44, off
	global_store_short v[46:47], v45, off
